# expert conversion rewrite plus non-temporal stores in the P10 down-projection epilogue
# speedup vs baseline: 1.0080x; 1.0080x over previous
.LBB0_1473:
	v_mov_b32_e32 v19, v187
	v_mov_b32_e32 v17, v186
	s_nop 15
	s_nop 15
	s_nop 15
	s_nop 15
	v_pk_mul_f32 v[24:25], v[140:141], s[30:31] op_sel_hi:[1,0]
	v_lshl_add_u32 v18, v17, 4, v19
	v_ashrrev_i32_e32 v18, 2, v18
	v_and_b32_e32 v20, 3, v19
	v_mul_lo_u32 v21, v19, s71
	v_lshlrev_b32_e32 v17, 3, v17
	v_add3_u32 v17, s68, v21, v17
	v_mul_lo_u32 v21, v18, s71
	v_lshlrev_b32_e32 v20, 4, v20
	v_add3_u32 v22, s68, v21, v20
	v_lshlrev_b32_e32 v20, 6, v19
	v_and_b32_e32 v180, 0x80, v20
	v_pk_mul_f32 v[20:21], v[136:137], s[30:31] op_sel_hi:[1,0]
	v_mov_b32_e32 v26, v181
	v_mov_b32_e32 v27, v181
	v_cvt_pk_fp8_f32 v26, v20, v21
	v_cvt_pk_fp8_f32 v27, v24, v25
	v_pk_mul_f32 v[20:21], v[138:139], s[30:31] op_sel_hi:[1,0]
	v_pk_mul_f32 v[24:25], v[142:143], s[30:31] op_sel_hi:[1,0]
	v_cvt_pk_fp8_f32 v26, v20, v21 op_sel:[0,0,1]
	v_cvt_pk_fp8_f32 v27, v24, v25 op_sel:[0,0,1]
	v_pk_mul_f32 v[20:21], v[160:161], s[30:31] op_sel_hi:[1,0]
	v_pk_mul_f32 v[24:25], v[164:165], s[30:31] op_sel_hi:[1,0]
	v_mov_b32_e32 v28, v181
	v_mov_b32_e32 v29, v181
	v_cvt_pk_fp8_f32 v28, v20, v21
	v_cvt_pk_fp8_f32 v29, v24, v25
	v_pk_mul_f32 v[30:31], v[120:121], s[30:31] op_sel_hi:[1,0]
	v_pk_mul_f32 v[32:33], v[124:125], s[30:31] op_sel_hi:[1,0]
	v_mov_b32_e32 v34, v181
	v_mov_b32_e32 v35, v181
	v_cvt_pk_fp8_f32 v34, v30, v31
	v_cvt_pk_fp8_f32 v35, v32, v33
	s_lshl_b32 s6, s42, 8
	v_pk_mul_f32 v[20:21], v[162:163], s[30:31] op_sel_hi:[1,0]
	v_pk_mul_f32 v[24:25], v[166:167], s[30:31] op_sel_hi:[1,0]
	s_add_i32 s6, s6, s65
	v_cvt_pk_fp8_f32 v28, v20, v21 op_sel:[0,0,1]
	v_cvt_pk_fp8_f32 v29, v24, v25 op_sel:[0,0,1]
	v_pk_mul_f32 v[30:31], v[122:123], s[30:31] op_sel_hi:[1,0]
	v_pk_mul_f32 v[32:33], v[126:127], s[30:31] op_sel_hi:[1,0]
	v_add_u32_e32 v18, s6, v18
	v_lshlrev_b32_e32 v19, 4, v19
	v_cvt_pk_fp8_f32 v34, v30, v31 op_sel:[0,0,1]
	v_cvt_pk_fp8_f32 v35, v32, v33 op_sel:[0,0,1]
	v_pk_mul_f32 v[30:31], v[144:145], s[30:31] op_sel_hi:[1,0]
	v_pk_mul_f32 v[32:33], v[152:153], s[30:31] op_sel_hi:[1,0]
	v_mov_b32_e32 v36, v181
	v_mov_b32_e32 v37, v181
	v_and_b32_e32 v20, 16, v19
	v_ashrrev_i32_e32 v19, 31, v18
	v_cvt_pk_fp8_f32 v36, v30, v31
	v_cvt_pk_fp8_f32 v37, v32, v33
	s_lshl_b32 s6, s44, 8
	ds_write_b64 v17, v[26:27]
	ds_write_b64 v17, v[28:29] offset:32
	v_lshlrev_b64 v[28:29], 11, v[18:19]
	s_ashr_i32 s7, s6, 31
	ds_read_b128 v[24:27], v22
	v_lshl_add_u64 v[28:29], s[20:21], 0, v[28:29]
	v_lshl_add_u64 v[28:29], v[28:29], 0, s[6:7]
	v_pk_mul_f32 v[30:31], v[146:147], s[30:31] op_sel_hi:[1,0]
	v_pk_mul_f32 v[32:33], v[154:155], s[30:31] op_sel_hi:[1,0]
	v_lshl_add_u64 v[28:29], v[28:29], 0, v[180:181]
	v_cvt_pk_fp8_f32 v36, v30, v31 op_sel:[0,0,1]
	v_cvt_pk_fp8_f32 v37, v32, v33 op_sel:[0,0,1]
	v_mov_b32_e32 v21, v181
	v_lshl_add_u64 v[28:29], v[28:29], 0, s[18:19]
	v_lshl_add_u64 v[28:29], v[28:29], 0, v[20:21]
	s_waitcnt lgkmcnt(0)
	global_store_dwordx4 v[28:29], v[24:27], off nt
	ds_write_b64 v17, v[34:35]
	ds_write_b64 v17, v[36:37] offset:32
	v_pk_mul_f32 v[30:31], v[96:97], s[30:31] op_sel_hi:[1,0]
	v_pk_mul_f32 v[32:33], v[100:101], s[30:31] op_sel_hi:[1,0]
	v_mov_b32_e32 v34, v181
	v_mov_b32_e32 v35, v181
	v_cvt_pk_fp8_f32 v34, v30, v31
	v_cvt_pk_fp8_f32 v35, v32, v33
	v_pk_mul_f32 v[30:31], v[98:99], s[30:31] op_sel_hi:[1,0]
	v_pk_mul_f32 v[32:33], v[102:103], s[30:31] op_sel_hi:[1,0]
	v_add_u32_e32 v28, 16, v18
	v_cvt_pk_fp8_f32 v34, v30, v31 op_sel:[0,0,1]
	v_cvt_pk_fp8_f32 v35, v32, v33 op_sel:[0,0,1]
	v_pk_mul_f32 v[30:31], v[128:129], s[30:31] op_sel_hi:[1,0]
	v_pk_mul_f32 v[32:33], v[132:133], s[30:31] op_sel_hi:[1,0]
	v_mov_b32_e32 v36, v181
	v_mov_b32_e32 v37, v181
	v_ashrrev_i32_e32 v29, 31, v28
	v_cvt_pk_fp8_f32 v36, v30, v31
	v_cvt_pk_fp8_f32 v37, v32, v33
	v_lshlrev_b64 v[28:29], 11, v[28:29]
	ds_read_b128 v[24:27], v22
	v_lshl_add_u64 v[28:29], s[20:21], 0, v[28:29]
	v_lshl_add_u64 v[28:29], v[28:29], 0, s[6:7]
	v_pk_mul_f32 v[30:31], v[130:131], s[30:31] op_sel_hi:[1,0]
	v_pk_mul_f32 v[32:33], v[134:135], s[30:31] op_sel_hi:[1,0]
	v_lshl_add_u64 v[28:29], v[28:29], 0, v[180:181]
	v_cvt_pk_fp8_f32 v36, v30, v31 op_sel:[0,0,1]
	v_cvt_pk_fp8_f32 v37, v32, v33 op_sel:[0,0,1]
	v_lshl_add_u64 v[28:29], v[28:29], 0, s[18:19]
	v_lshl_add_u64 v[28:29], v[28:29], 0, v[20:21]
	s_waitcnt lgkmcnt(0)
	global_store_dwordx4 v[28:29], v[24:27], off nt
	ds_write_b64 v17, v[34:35]
	ds_write_b64 v17, v[36:37] offset:32
	v_pk_mul_f32 v[30:31], v[80:81], s[30:31] op_sel_hi:[1,0]
	v_pk_mul_f32 v[32:33], v[84:85], s[30:31] op_sel_hi:[1,0]
	v_mov_b32_e32 v34, v181
	v_mov_b32_e32 v35, v181
	v_cvt_pk_fp8_f32 v34, v30, v31
	v_cvt_pk_fp8_f32 v35, v32, v33
	v_pk_mul_f32 v[30:31], v[82:83], s[30:31] op_sel_hi:[1,0]
	v_pk_mul_f32 v[32:33], v[86:87], s[30:31] op_sel_hi:[1,0]
	v_add_u32_e32 v28, 32, v18
	v_cvt_pk_fp8_f32 v34, v30, v31 op_sel:[0,0,1]
	v_cvt_pk_fp8_f32 v35, v32, v33 op_sel:[0,0,1]
	v_pk_mul_f32 v[30:31], v[104:105], s[30:31] op_sel_hi:[1,0]
	v_pk_mul_f32 v[32:33], v[112:113], s[30:31] op_sel_hi:[1,0]
	v_mov_b32_e32 v36, v181
	v_mov_b32_e32 v37, v181
	v_ashrrev_i32_e32 v29, 31, v28
	v_cvt_pk_fp8_f32 v36, v30, v31
	v_cvt_pk_fp8_f32 v37, v32, v33
	v_lshlrev_b64 v[28:29], 11, v[28:29]
	ds_read_b128 v[24:27], v22
	v_lshl_add_u64 v[28:29], s[20:21], 0, v[28:29]
	v_lshl_add_u64 v[28:29], v[28:29], 0, s[6:7]
	v_pk_mul_f32 v[30:31], v[106:107], s[30:31] op_sel_hi:[1,0]
	v_pk_mul_f32 v[32:33], v[114:115], s[30:31] op_sel_hi:[1,0]
	v_lshl_add_u64 v[28:29], v[28:29], 0, v[180:181]
	v_cvt_pk_fp8_f32 v36, v30, v31 op_sel:[0,0,1]
	v_cvt_pk_fp8_f32 v37, v32, v33 op_sel:[0,0,1]
	v_lshl_add_u64 v[28:29], v[28:29], 0, s[18:19]
	v_lshl_add_u64 v[28:29], v[28:29], 0, v[20:21]
	s_waitcnt lgkmcnt(0)
	global_store_dwordx4 v[28:29], v[24:27], off nt
	ds_write_b64 v17, v[34:35]
	ds_write_b64 v17, v[36:37] offset:32
	v_pk_mul_f32 v[30:31], v[108:109], s[30:31] op_sel_hi:[1,0]
	v_pk_mul_f32 v[32:33], v[116:117], s[30:31] op_sel_hi:[1,0]
	v_mov_b32_e32 v34, v181
	v_mov_b32_e32 v35, v181
	v_cvt_pk_fp8_f32 v34, v30, v31
	v_cvt_pk_fp8_f32 v35, v32, v33
	v_pk_mul_f32 v[30:31], v[110:111], s[30:31] op_sel_hi:[1,0]
	v_pk_mul_f32 v[32:33], v[118:119], s[30:31] op_sel_hi:[1,0]
	v_add_u32_e32 v28, 48, v18
	v_cvt_pk_fp8_f32 v34, v30, v31 op_sel:[0,0,1]
	v_cvt_pk_fp8_f32 v35, v32, v33 op_sel:[0,0,1]
	v_pk_mul_f32 v[30:31], v[148:149], s[30:31] op_sel_hi:[1,0]
	v_pk_mul_f32 v[32:33], v[156:157], s[30:31] op_sel_hi:[1,0]
	v_mov_b32_e32 v36, v181
	v_mov_b32_e32 v37, v181
	v_ashrrev_i32_e32 v29, 31, v28
	v_cvt_pk_fp8_f32 v36, v30, v31
	v_cvt_pk_fp8_f32 v37, v32, v33
	v_lshlrev_b64 v[28:29], 11, v[28:29]
	ds_read_b128 v[24:27], v22
	v_lshl_add_u64 v[28:29], s[20:21], 0, v[28:29]
	v_lshl_add_u64 v[28:29], v[28:29], 0, s[6:7]
	v_pk_mul_f32 v[30:31], v[150:151], s[30:31] op_sel_hi:[1,0]
	v_pk_mul_f32 v[32:33], v[158:159], s[30:31] op_sel_hi:[1,0]
	v_lshl_add_u64 v[28:29], v[28:29], 0, v[180:181]
	v_cvt_pk_fp8_f32 v36, v30, v31 op_sel:[0,0,1]
	v_cvt_pk_fp8_f32 v37, v32, v33 op_sel:[0,0,1]
	v_lshl_add_u64 v[28:29], v[28:29], 0, s[18:19]
	v_lshl_add_u64 v[28:29], v[28:29], 0, v[20:21]
	s_waitcnt lgkmcnt(0)
	global_store_dwordx4 v[28:29], v[24:27], off nt
	ds_write_b64 v17, v[34:35]
	ds_write_b64 v17, v[36:37] offset:32
	v_pk_mul_f32 v[30:31], v[88:89], s[30:31] op_sel_hi:[1,0]
	v_pk_mul_f32 v[32:33], v[92:93], s[30:31] op_sel_hi:[1,0]
	v_mov_b32_e32 v34, v181
	v_mov_b32_e32 v35, v181
	v_cvt_pk_fp8_f32 v34, v30, v31
	v_cvt_pk_fp8_f32 v35, v32, v33
	v_pk_mul_f32 v[30:31], v[90:91], s[30:31] op_sel_hi:[1,0]
	v_pk_mul_f32 v[32:33], v[94:95], s[30:31] op_sel_hi:[1,0]
	v_add_u32_e32 v28, 0x80, v18
	v_cvt_pk_fp8_f32 v34, v30, v31 op_sel:[0,0,1]
	v_cvt_pk_fp8_f32 v35, v32, v33 op_sel:[0,0,1]
	v_pk_mul_f32 v[30:31], v[56:57], s[30:31] op_sel_hi:[1,0]
	v_pk_mul_f32 v[32:33], v[60:61], s[30:31] op_sel_hi:[1,0]
	v_mov_b32_e32 v36, v181
	v_mov_b32_e32 v37, v181
	v_ashrrev_i32_e32 v29, 31, v28
	v_cvt_pk_fp8_f32 v36, v30, v31
	v_cvt_pk_fp8_f32 v37, v32, v33
	v_lshlrev_b64 v[28:29], 11, v[28:29]
	ds_read_b128 v[24:27], v22
	v_lshl_add_u64 v[28:29], s[20:21], 0, v[28:29]
	v_lshl_add_u64 v[28:29], v[28:29], 0, s[6:7]
	v_pk_mul_f32 v[30:31], v[58:59], s[30:31] op_sel_hi:[1,0]
	v_pk_mul_f32 v[32:33], v[62:63], s[30:31] op_sel_hi:[1,0]
	v_lshl_add_u64 v[28:29], v[28:29], 0, v[180:181]
	v_cvt_pk_fp8_f32 v36, v30, v31 op_sel:[0,0,1]
	v_cvt_pk_fp8_f32 v37, v32, v33 op_sel:[0,0,1]
	v_lshl_add_u64 v[28:29], v[28:29], 0, s[18:19]
	v_lshl_add_u64 v[28:29], v[28:29], 0, v[20:21]
	s_waitcnt lgkmcnt(0)
	global_store_dwordx4 v[28:29], v[24:27], off nt
	ds_write_b64 v17, v[34:35]
	ds_write_b64 v17, v[36:37] offset:32
	v_pk_mul_f32 v[30:31], v[72:73], s[30:31] op_sel_hi:[1,0]
	v_mov_b32_e32 v34, v181
	v_cvt_pk_fp8_f32 v34, v30, v31
	v_add_u32_e32 v28, 0x90, v18
	v_ashrrev_i32_e32 v29, 31, v28
	v_pk_mul_f32 v[30:31], v[74:75], s[30:31] op_sel_hi:[1,0]
	v_lshlrev_b64 v[28:29], 11, v[28:29]
	v_cvt_pk_fp8_f32 v34, v30, v31 op_sel:[0,0,1]
	v_pk_mul_f32 v[8:9], v[8:9], s[30:31] op_sel_hi:[1,0]
	v_mov_b32_e32 v30, v181
	ds_read_b128 v[24:27], v22
	v_lshl_add_u64 v[28:29], s[20:21], 0, v[28:29]
	v_cvt_pk_fp8_f32 v30, v8, v9
	v_lshl_add_u64 v[28:29], v[28:29], 0, s[6:7]
	v_lshl_add_u64 v[28:29], v[28:29], 0, v[180:181]
	v_lshl_add_u64 v[28:29], v[28:29], 0, s[18:19]
	v_pk_mul_f32 v[32:33], v[76:77], s[30:31] op_sel_hi:[1,0]
	v_mov_b32_e32 v35, v181
	v_pk_mul_f32 v[8:9], v[10:11], s[30:31] op_sel_hi:[1,0]
	v_cvt_pk_fp8_f32 v35, v32, v33
	v_pk_mul_f32 v[12:13], v[12:13], s[30:31] op_sel_hi:[1,0]
	v_mov_b32_e32 v31, v181
	v_cvt_pk_fp8_f32 v30, v8, v9 op_sel:[0,0,1]
	v_lshl_add_u64 v[8:9], v[28:29], 0, v[20:21]
	v_cvt_pk_fp8_f32 v31, v12, v13
	v_pk_mul_f32 v[10:11], v[14:15], s[30:31] op_sel_hi:[1,0]
	s_waitcnt lgkmcnt(0)
	global_store_dwordx4 v[8:9], v[24:27], off nt
	v_pk_mul_f32 v[14:15], v[68:69], s[30:31] op_sel_hi:[1,0]
	v_pk_mul_f32 v[32:33], v[78:79], s[30:31] op_sel_hi:[1,0]
	v_mov_b32_e32 v26, v181
	v_cvt_pk_fp8_f32 v26, v14, v15
	v_cvt_pk_fp8_f32 v35, v32, v33 op_sel:[0,0,1]
	v_cvt_pk_fp8_f32 v31, v10, v11 op_sel:[0,0,1]
	v_pk_mul_f32 v[24:25], v[64:65], s[30:31] op_sel_hi:[1,0]
	v_mov_b32_e32 v27, v181
	v_pk_mul_f32 v[14:15], v[70:71], s[30:31] op_sel_hi:[1,0]
	v_add_u32_e32 v12, 0xa0, v18
	v_cvt_pk_fp8_f32 v27, v24, v25
	v_cvt_pk_fp8_f32 v26, v14, v15 op_sel:[0,0,1]
	v_pk_mul_f32 v[4:5], v[4:5], s[30:31] op_sel_hi:[1,0]
	v_pk_mul_f32 v[0:1], v[0:1], s[30:31] op_sel_hi:[1,0]
	v_mov_b32_e32 v14, v181
	v_mov_b32_e32 v15, v181
	v_ashrrev_i32_e32 v13, 31, v12
	v_cvt_pk_fp8_f32 v14, v4, v5
	v_cvt_pk_fp8_f32 v15, v0, v1
	ds_write_b64 v17, v[34:35]
	ds_write_b64 v17, v[30:31] offset:32
	v_lshlrev_b64 v[12:13], 11, v[12:13]
	ds_read_b128 v[8:11], v22
	v_lshl_add_u64 v[12:13], s[20:21], 0, v[12:13]
	v_pk_mul_f32 v[24:25], v[66:67], s[30:31] op_sel_hi:[1,0]
	v_lshl_add_u64 v[12:13], v[12:13], 0, s[6:7]
	v_cvt_pk_fp8_f32 v27, v24, v25 op_sel:[0,0,1]
	v_pk_mul_f32 v[0:1], v[6:7], s[30:31] op_sel_hi:[1,0]
	v_pk_mul_f32 v[2:3], v[2:3], s[30:31] op_sel_hi:[1,0]
	v_lshl_add_u64 v[12:13], v[12:13], 0, v[180:181]
	v_cvt_pk_fp8_f32 v14, v0, v1 op_sel:[0,0,1]
	v_cvt_pk_fp8_f32 v15, v2, v3 op_sel:[0,0,1]
	v_lshl_add_u64 v[12:13], v[12:13], 0, s[18:19]
	v_add_u32_e32 v4, 0xb0, v18
	v_lshl_add_u64 v[0:1], v[12:13], 0, v[20:21]
	v_ashrrev_i32_e32 v5, 31, v4
	s_waitcnt lgkmcnt(0)
	global_store_dwordx4 v[0:1], v[8:11], off nt
	ds_write_b64 v17, v[26:27]
	ds_write_b64 v17, v[14:15] offset:32
	v_lshlrev_b64 v[4:5], 11, v[4:5]
	ds_read_b128 v[0:3], v22
	v_lshl_add_u64 v[4:5], s[20:21], 0, v[4:5]
	v_lshl_add_u64 v[4:5], v[4:5], 0, s[6:7]
	v_lshl_add_u64 v[4:5], v[4:5], 0, v[180:181]
	v_lshl_add_u64 v[4:5], v[4:5], 0, s[18:19]
	v_lshl_add_u64 v[4:5], v[4:5], 0, v[20:21]
	s_mov_b64 s[6:7], -1
	s_andn2_b64 vcc, exec, s[4:5]
	s_mov_b32 s44, s36
	s_mov_b32 s42, s34
	s_mov_b64 s[48:49], s[40:41]
	s_mov_b64 s[50:51], s[38:39]
	s_waitcnt lgkmcnt(0)
	global_store_dwordx4 v[4:5], v[0:3], off nt
	s_cbranch_vccz .LBB0_1488

.LBB0_2750:
	v_mov_b32_e32 v17, v186
	v_mov_b32_e32 v19, v187
	s_nop 15
	s_nop 15
	s_nop 15
	s_nop 15
	v_pk_mul_f32 v[24:25], v[140:141], s[30:31] op_sel_hi:[1,0]
	v_lshl_add_u32 v18, v17, 4, v19
	v_ashrrev_i32_e32 v18, 2, v18
	v_and_b32_e32 v20, 3, v19
	v_mul_lo_u32 v21, v19, s71
	v_lshlrev_b32_e32 v17, 3, v17
	v_add3_u32 v17, s68, v21, v17
	v_mul_lo_u32 v21, v18, s71
	v_lshlrev_b32_e32 v20, 4, v20
	v_add3_u32 v22, s68, v21, v20
	v_lshlrev_b32_e32 v20, 6, v19
	v_and_b32_e32 v180, 0x80, v20
	v_pk_mul_f32 v[20:21], v[136:137], s[30:31] op_sel_hi:[1,0]
	v_mov_b32_e32 v26, v181
	v_mov_b32_e32 v27, v181
	v_cvt_pk_fp8_f32 v26, v20, v21
	v_cvt_pk_fp8_f32 v27, v24, v25
	v_pk_mul_f32 v[20:21], v[138:139], s[30:31] op_sel_hi:[1,0]
	v_pk_mul_f32 v[24:25], v[142:143], s[30:31] op_sel_hi:[1,0]
	v_cvt_pk_fp8_f32 v26, v20, v21 op_sel:[0,0,1]
	v_cvt_pk_fp8_f32 v27, v24, v25 op_sel:[0,0,1]
	v_pk_mul_f32 v[20:21], v[160:161], s[30:31] op_sel_hi:[1,0]
	v_pk_mul_f32 v[24:25], v[164:165], s[30:31] op_sel_hi:[1,0]
	v_mov_b32_e32 v28, v181
	v_mov_b32_e32 v29, v181
	v_cvt_pk_fp8_f32 v28, v20, v21
	v_cvt_pk_fp8_f32 v29, v24, v25
	v_pk_mul_f32 v[30:31], v[120:121], s[30:31] op_sel_hi:[1,0]
	v_pk_mul_f32 v[32:33], v[124:125], s[30:31] op_sel_hi:[1,0]
	v_mov_b32_e32 v34, v181
	v_mov_b32_e32 v35, v181
	v_cvt_pk_fp8_f32 v34, v30, v31
	v_cvt_pk_fp8_f32 v35, v32, v33
	s_lshl_b32 s6, s42, 8
	v_pk_mul_f32 v[20:21], v[162:163], s[30:31] op_sel_hi:[1,0]
	v_pk_mul_f32 v[24:25], v[166:167], s[30:31] op_sel_hi:[1,0]
	s_add_i32 s6, s6, s65
	v_cvt_pk_fp8_f32 v28, v20, v21 op_sel:[0,0,1]
	v_cvt_pk_fp8_f32 v29, v24, v25 op_sel:[0,0,1]
	v_pk_mul_f32 v[30:31], v[122:123], s[30:31] op_sel_hi:[1,0]
	v_pk_mul_f32 v[32:33], v[126:127], s[30:31] op_sel_hi:[1,0]
	v_add_u32_e32 v18, s6, v18
	v_lshlrev_b32_e32 v19, 4, v19
	v_cvt_pk_fp8_f32 v34, v30, v31 op_sel:[0,0,1]
	v_cvt_pk_fp8_f32 v35, v32, v33 op_sel:[0,0,1]
	v_pk_mul_f32 v[30:31], v[144:145], s[30:31] op_sel_hi:[1,0]
	v_pk_mul_f32 v[32:33], v[152:153], s[30:31] op_sel_hi:[1,0]
	v_mov_b32_e32 v36, v181
	v_mov_b32_e32 v37, v181
	v_and_b32_e32 v20, 16, v19
	v_ashrrev_i32_e32 v19, 31, v18
	v_cvt_pk_fp8_f32 v36, v30, v31
	v_cvt_pk_fp8_f32 v37, v32, v33
	s_lshl_b32 s6, s44, 8
	ds_write_b64 v17, v[26:27]
	ds_write_b64 v17, v[28:29] offset:32
	v_lshlrev_b64 v[28:29], 11, v[18:19]
	s_ashr_i32 s7, s6, 31
	ds_read_b128 v[24:27], v22
	v_lshl_add_u64 v[28:29], s[20:21], 0, v[28:29]
	v_lshl_add_u64 v[28:29], v[28:29], 0, s[6:7]
	v_pk_mul_f32 v[30:31], v[146:147], s[30:31] op_sel_hi:[1,0]
	v_pk_mul_f32 v[32:33], v[154:155], s[30:31] op_sel_hi:[1,0]
	v_lshl_add_u64 v[28:29], v[28:29], 0, v[180:181]
	v_cvt_pk_fp8_f32 v36, v30, v31 op_sel:[0,0,1]
	v_cvt_pk_fp8_f32 v37, v32, v33 op_sel:[0,0,1]
	v_mov_b32_e32 v21, v181
	v_lshl_add_u64 v[28:29], v[28:29], 0, s[18:19]
	v_lshl_add_u64 v[28:29], v[28:29], 0, v[20:21]
	s_waitcnt lgkmcnt(0)
	global_store_dwordx4 v[28:29], v[24:27], off nt
	ds_write_b64 v17, v[34:35]
	ds_write_b64 v17, v[36:37] offset:32
	v_pk_mul_f32 v[30:31], v[96:97], s[30:31] op_sel_hi:[1,0]
	v_pk_mul_f32 v[32:33], v[100:101], s[30:31] op_sel_hi:[1,0]
	v_mov_b32_e32 v34, v181
	v_mov_b32_e32 v35, v181
	v_cvt_pk_fp8_f32 v34, v30, v31
	v_cvt_pk_fp8_f32 v35, v32, v33
	v_pk_mul_f32 v[30:31], v[98:99], s[30:31] op_sel_hi:[1,0]
	v_pk_mul_f32 v[32:33], v[102:103], s[30:31] op_sel_hi:[1,0]
	v_add_u32_e32 v28, 16, v18
	v_cvt_pk_fp8_f32 v34, v30, v31 op_sel:[0,0,1]
	v_cvt_pk_fp8_f32 v35, v32, v33 op_sel:[0,0,1]
	v_pk_mul_f32 v[30:31], v[128:129], s[30:31] op_sel_hi:[1,0]
	v_pk_mul_f32 v[32:33], v[132:133], s[30:31] op_sel_hi:[1,0]
	v_mov_b32_e32 v36, v181
	v_mov_b32_e32 v37, v181
	v_ashrrev_i32_e32 v29, 31, v28
	v_cvt_pk_fp8_f32 v36, v30, v31
	v_cvt_pk_fp8_f32 v37, v32, v33
	v_lshlrev_b64 v[28:29], 11, v[28:29]
	ds_read_b128 v[24:27], v22
	v_lshl_add_u64 v[28:29], s[20:21], 0, v[28:29]
	v_lshl_add_u64 v[28:29], v[28:29], 0, s[6:7]
	v_pk_mul_f32 v[30:31], v[130:131], s[30:31] op_sel_hi:[1,0]
	v_pk_mul_f32 v[32:33], v[134:135], s[30:31] op_sel_hi:[1,0]
	v_lshl_add_u64 v[28:29], v[28:29], 0, v[180:181]
	v_cvt_pk_fp8_f32 v36, v30, v31 op_sel:[0,0,1]
	v_cvt_pk_fp8_f32 v37, v32, v33 op_sel:[0,0,1]
	v_lshl_add_u64 v[28:29], v[28:29], 0, s[18:19]
	v_lshl_add_u64 v[28:29], v[28:29], 0, v[20:21]
	s_waitcnt lgkmcnt(0)
	global_store_dwordx4 v[28:29], v[24:27], off nt
	ds_write_b64 v17, v[34:35]
	ds_write_b64 v17, v[36:37] offset:32
	v_pk_mul_f32 v[30:31], v[80:81], s[30:31] op_sel_hi:[1,0]
	v_pk_mul_f32 v[32:33], v[84:85], s[30:31] op_sel_hi:[1,0]
	v_mov_b32_e32 v34, v181
	v_mov_b32_e32 v35, v181
	v_cvt_pk_fp8_f32 v34, v30, v31
	v_cvt_pk_fp8_f32 v35, v32, v33
	v_pk_mul_f32 v[30:31], v[82:83], s[30:31] op_sel_hi:[1,0]
	v_pk_mul_f32 v[32:33], v[86:87], s[30:31] op_sel_hi:[1,0]
	v_add_u32_e32 v28, 32, v18
	v_cvt_pk_fp8_f32 v34, v30, v31 op_sel:[0,0,1]
	v_cvt_pk_fp8_f32 v35, v32, v33 op_sel:[0,0,1]
	v_pk_mul_f32 v[30:31], v[104:105], s[30:31] op_sel_hi:[1,0]
	v_pk_mul_f32 v[32:33], v[112:113], s[30:31] op_sel_hi:[1,0]
	v_mov_b32_e32 v36, v181
	v_mov_b32_e32 v37, v181
	v_ashrrev_i32_e32 v29, 31, v28
	v_cvt_pk_fp8_f32 v36, v30, v31
	v_cvt_pk_fp8_f32 v37, v32, v33
	v_lshlrev_b64 v[28:29], 11, v[28:29]
	ds_read_b128 v[24:27], v22
	v_lshl_add_u64 v[28:29], s[20:21], 0, v[28:29]
	v_lshl_add_u64 v[28:29], v[28:29], 0, s[6:7]
	v_pk_mul_f32 v[30:31], v[106:107], s[30:31] op_sel_hi:[1,0]
	v_pk_mul_f32 v[32:33], v[114:115], s[30:31] op_sel_hi:[1,0]
	v_lshl_add_u64 v[28:29], v[28:29], 0, v[180:181]
	v_cvt_pk_fp8_f32 v36, v30, v31 op_sel:[0,0,1]
	v_cvt_pk_fp8_f32 v37, v32, v33 op_sel:[0,0,1]
	v_lshl_add_u64 v[28:29], v[28:29], 0, s[18:19]
	v_lshl_add_u64 v[28:29], v[28:29], 0, v[20:21]
	s_waitcnt lgkmcnt(0)
	global_store_dwordx4 v[28:29], v[24:27], off nt
	ds_write_b64 v17, v[34:35]
	ds_write_b64 v17, v[36:37] offset:32
	v_pk_mul_f32 v[30:31], v[108:109], s[30:31] op_sel_hi:[1,0]
	v_pk_mul_f32 v[32:33], v[116:117], s[30:31] op_sel_hi:[1,0]
	v_mov_b32_e32 v34, v181
	v_mov_b32_e32 v35, v181
	v_cvt_pk_fp8_f32 v34, v30, v31
	v_cvt_pk_fp8_f32 v35, v32, v33
	v_pk_mul_f32 v[30:31], v[110:111], s[30:31] op_sel_hi:[1,0]
	v_pk_mul_f32 v[32:33], v[118:119], s[30:31] op_sel_hi:[1,0]
	v_add_u32_e32 v28, 48, v18
	v_cvt_pk_fp8_f32 v34, v30, v31 op_sel:[0,0,1]
	v_cvt_pk_fp8_f32 v35, v32, v33 op_sel:[0,0,1]
	v_pk_mul_f32 v[30:31], v[148:149], s[30:31] op_sel_hi:[1,0]
	v_pk_mul_f32 v[32:33], v[156:157], s[30:31] op_sel_hi:[1,0]
	v_mov_b32_e32 v36, v181
	v_mov_b32_e32 v37, v181
	v_ashrrev_i32_e32 v29, 31, v28
	v_cvt_pk_fp8_f32 v36, v30, v31
	v_cvt_pk_fp8_f32 v37, v32, v33
	v_lshlrev_b64 v[28:29], 11, v[28:29]
	ds_read_b128 v[24:27], v22
	v_lshl_add_u64 v[28:29], s[20:21], 0, v[28:29]
	v_lshl_add_u64 v[28:29], v[28:29], 0, s[6:7]
	v_pk_mul_f32 v[30:31], v[150:151], s[30:31] op_sel_hi:[1,0]
	v_pk_mul_f32 v[32:33], v[158:159], s[30:31] op_sel_hi:[1,0]
	v_lshl_add_u64 v[28:29], v[28:29], 0, v[180:181]
	v_cvt_pk_fp8_f32 v36, v30, v31 op_sel:[0,0,1]
	v_cvt_pk_fp8_f32 v37, v32, v33 op_sel:[0,0,1]
	v_lshl_add_u64 v[28:29], v[28:29], 0, s[18:19]
	v_lshl_add_u64 v[28:29], v[28:29], 0, v[20:21]
	s_waitcnt lgkmcnt(0)
	global_store_dwordx4 v[28:29], v[24:27], off nt
	ds_write_b64 v17, v[34:35]
	ds_write_b64 v17, v[36:37] offset:32
	v_pk_mul_f32 v[30:31], v[88:89], s[30:31] op_sel_hi:[1,0]
	v_pk_mul_f32 v[32:33], v[92:93], s[30:31] op_sel_hi:[1,0]
	v_mov_b32_e32 v34, v181
	v_mov_b32_e32 v35, v181
	v_cvt_pk_fp8_f32 v34, v30, v31
	v_cvt_pk_fp8_f32 v35, v32, v33
	v_pk_mul_f32 v[30:31], v[90:91], s[30:31] op_sel_hi:[1,0]
	v_pk_mul_f32 v[32:33], v[94:95], s[30:31] op_sel_hi:[1,0]
	v_add_u32_e32 v28, 0x80, v18
	v_cvt_pk_fp8_f32 v34, v30, v31 op_sel:[0,0,1]
	v_cvt_pk_fp8_f32 v35, v32, v33 op_sel:[0,0,1]
	v_pk_mul_f32 v[30:31], v[56:57], s[30:31] op_sel_hi:[1,0]
	v_pk_mul_f32 v[32:33], v[60:61], s[30:31] op_sel_hi:[1,0]
	v_mov_b32_e32 v36, v181
	v_mov_b32_e32 v37, v181
	v_ashrrev_i32_e32 v29, 31, v28
	v_cvt_pk_fp8_f32 v36, v30, v31
	v_cvt_pk_fp8_f32 v37, v32, v33
	v_lshlrev_b64 v[28:29], 11, v[28:29]
	ds_read_b128 v[24:27], v22
	v_lshl_add_u64 v[28:29], s[20:21], 0, v[28:29]
	v_lshl_add_u64 v[28:29], v[28:29], 0, s[6:7]
	v_pk_mul_f32 v[30:31], v[58:59], s[30:31] op_sel_hi:[1,0]
	v_pk_mul_f32 v[32:33], v[62:63], s[30:31] op_sel_hi:[1,0]
	v_lshl_add_u64 v[28:29], v[28:29], 0, v[180:181]
	v_cvt_pk_fp8_f32 v36, v30, v31 op_sel:[0,0,1]
	v_cvt_pk_fp8_f32 v37, v32, v33 op_sel:[0,0,1]
	v_lshl_add_u64 v[28:29], v[28:29], 0, s[18:19]
	v_lshl_add_u64 v[28:29], v[28:29], 0, v[20:21]
	s_waitcnt lgkmcnt(0)
	global_store_dwordx4 v[28:29], v[24:27], off nt
	ds_write_b64 v17, v[34:35]
	ds_write_b64 v17, v[36:37] offset:32
	v_pk_mul_f32 v[30:31], v[72:73], s[30:31] op_sel_hi:[1,0]
	v_mov_b32_e32 v34, v181
	v_cvt_pk_fp8_f32 v34, v30, v31
	v_add_u32_e32 v28, 0x90, v18
	v_ashrrev_i32_e32 v29, 31, v28
	v_pk_mul_f32 v[30:31], v[74:75], s[30:31] op_sel_hi:[1,0]
	v_lshlrev_b64 v[28:29], 11, v[28:29]
	v_cvt_pk_fp8_f32 v34, v30, v31 op_sel:[0,0,1]
	v_pk_mul_f32 v[8:9], v[8:9], s[30:31] op_sel_hi:[1,0]
	v_mov_b32_e32 v30, v181
	ds_read_b128 v[24:27], v22
	v_lshl_add_u64 v[28:29], s[20:21], 0, v[28:29]
	v_cvt_pk_fp8_f32 v30, v8, v9
	v_lshl_add_u64 v[28:29], v[28:29], 0, s[6:7]
	v_lshl_add_u64 v[28:29], v[28:29], 0, v[180:181]
	v_lshl_add_u64 v[28:29], v[28:29], 0, s[18:19]
	v_pk_mul_f32 v[32:33], v[76:77], s[30:31] op_sel_hi:[1,0]
	v_mov_b32_e32 v35, v181
	v_pk_mul_f32 v[8:9], v[10:11], s[30:31] op_sel_hi:[1,0]
	v_cvt_pk_fp8_f32 v35, v32, v33
	v_pk_mul_f32 v[12:13], v[12:13], s[30:31] op_sel_hi:[1,0]
	v_mov_b32_e32 v31, v181
	v_cvt_pk_fp8_f32 v30, v8, v9 op_sel:[0,0,1]
	v_lshl_add_u64 v[8:9], v[28:29], 0, v[20:21]
	v_cvt_pk_fp8_f32 v31, v12, v13
	v_pk_mul_f32 v[10:11], v[14:15], s[30:31] op_sel_hi:[1,0]
	s_waitcnt lgkmcnt(0)
	global_store_dwordx4 v[8:9], v[24:27], off nt
	v_pk_mul_f32 v[14:15], v[68:69], s[30:31] op_sel_hi:[1,0]
	v_pk_mul_f32 v[32:33], v[78:79], s[30:31] op_sel_hi:[1,0]
	v_mov_b32_e32 v26, v181
	v_cvt_pk_fp8_f32 v26, v14, v15
	v_cvt_pk_fp8_f32 v35, v32, v33 op_sel:[0,0,1]
	v_cvt_pk_fp8_f32 v31, v10, v11 op_sel:[0,0,1]
	v_pk_mul_f32 v[24:25], v[64:65], s[30:31] op_sel_hi:[1,0]
	v_mov_b32_e32 v27, v181
	v_pk_mul_f32 v[14:15], v[70:71], s[30:31] op_sel_hi:[1,0]
	v_add_u32_e32 v12, 0xa0, v18
	v_cvt_pk_fp8_f32 v27, v24, v25
	v_cvt_pk_fp8_f32 v26, v14, v15 op_sel:[0,0,1]
	v_pk_mul_f32 v[4:5], v[4:5], s[30:31] op_sel_hi:[1,0]
	v_pk_mul_f32 v[0:1], v[0:1], s[30:31] op_sel_hi:[1,0]
	v_mov_b32_e32 v14, v181
	v_mov_b32_e32 v15, v181
	v_ashrrev_i32_e32 v13, 31, v12
	v_cvt_pk_fp8_f32 v14, v4, v5
	v_cvt_pk_fp8_f32 v15, v0, v1
	ds_write_b64 v17, v[34:35]
	ds_write_b64 v17, v[30:31] offset:32
	v_lshlrev_b64 v[12:13], 11, v[12:13]
	ds_read_b128 v[8:11], v22
	v_lshl_add_u64 v[12:13], s[20:21], 0, v[12:13]
	v_pk_mul_f32 v[24:25], v[66:67], s[30:31] op_sel_hi:[1,0]
	v_lshl_add_u64 v[12:13], v[12:13], 0, s[6:7]
	v_cvt_pk_fp8_f32 v27, v24, v25 op_sel:[0,0,1]
	v_pk_mul_f32 v[0:1], v[6:7], s[30:31] op_sel_hi:[1,0]
	v_pk_mul_f32 v[2:3], v[2:3], s[30:31] op_sel_hi:[1,0]
	v_lshl_add_u64 v[12:13], v[12:13], 0, v[180:181]
	v_cvt_pk_fp8_f32 v14, v0, v1 op_sel:[0,0,1]
	v_cvt_pk_fp8_f32 v15, v2, v3 op_sel:[0,0,1]
	v_lshl_add_u64 v[12:13], v[12:13], 0, s[18:19]
	v_add_u32_e32 v4, 0xb0, v18
	v_lshl_add_u64 v[0:1], v[12:13], 0, v[20:21]
	v_ashrrev_i32_e32 v5, 31, v4
	s_waitcnt lgkmcnt(0)
	global_store_dwordx4 v[0:1], v[8:11], off nt
	ds_write_b64 v17, v[26:27]
	ds_write_b64 v17, v[14:15] offset:32
	v_lshlrev_b64 v[4:5], 11, v[4:5]
	ds_read_b128 v[0:3], v22
	v_lshl_add_u64 v[4:5], s[20:21], 0, v[4:5]
	v_lshl_add_u64 v[4:5], v[4:5], 0, s[6:7]
	v_lshl_add_u64 v[4:5], v[4:5], 0, v[180:181]
	v_lshl_add_u64 v[4:5], v[4:5], 0, s[18:19]
	v_lshl_add_u64 v[4:5], v[4:5], 0, v[20:21]
	s_mov_b64 s[6:7], -1
	s_andn2_b64 vcc, exec, s[4:5]
	s_mov_b32 s44, s36
	s_mov_b32 s42, s34
	s_mov_b64 s[48:49], s[40:41]
	s_mov_b64 s[50:51], s[38:39]
	s_waitcnt lgkmcnt(0)
	global_store_dwordx4 v[4:5], v[0:3], off nt
	s_cbranch_vccz .LBB0_2765
